# baseline (speedup 1.0000x reference)
.Lmy_noprio:
	s_lshl_b64 s[76:77], s[38:39], 18
	s_waitcnt lgkmcnt(0)
	s_bfe_u32 s100, s2, 0x30003
	s_sub_i32 s100, 15, s100
	s_add_i32 s101, s100, 1
	s_cmp_eq_u32 s33, 1
	s_cselect_b32 s101, s101, 0
	v_and_b32_e32 v255, 31, v0
	v_bfe_u32 v254, v0, 6, 2
	v_lshl_or_b32 v255, v254, 5, v255
	s_lshl_b32 s100, s100, 7
	v_add_u32_e32 v255, s100, v255
	v_lshlrev_b32_e32 v255, 7, v255
	v_and_b32_e32 v253, 63, v0
	v_lshlrev_b32_e32 v254, 7, v253
	v_lshlrev_b32_e32 v253, 12, v253
	s_lshl_b32 s100, s101, 13
	v_add_u32_e32 v254, s100, v254
	s_lshl_b32 s100, s101, 7
	v_add_u32_e32 v253, s100, v253
	s_add_u32 s100, s70, s76
	s_addc_u32 s101, s71, s77
	global_load_dword v254, v254, s[100:101]
	s_add_u32 s100, s72, s76
	s_addc_u32 s101, s73, s77
	global_load_dword v253, v253, s[100:101]
	s_add_u32 s100, s68, s76
	s_addc_u32 s101, s69, s77
	global_load_dword v255, v255, s[100:101]
	s_add_u32 s0, s70, s76
	v_bfe_u32 v4, v0, 5, 1
	v_and_b32_e32 v1, 63, v0
	v_writelane_b32 v252, s0, 0
	s_addc_u32 s0, s71, s77
	v_lshlrev_b32_e32 v159, 2, v4
	v_writelane_b32 v252, s0, 1
	v_cmp_gt_u32_e64 s[4:5], 32, v1
	v_sub_u32_e32 v3, v0, v159
	v_mov_b32_e32 v2, 0x3c00
	v_writelane_b32 v252, s4, 2
	v_lshlrev_b32_e32 v3, 2, v3
	v_or_b32_e32 v11, 1, v159
	s_lshl_b32 s40, s33, 16
	v_writelane_b32 v252, s5, 3
	v_cndmask_b32_e64 v2, 0, v2, s[4:5]
	s_lshr_b32 s41, s1, 6
	s_bfe_u32 s5, s2, 0x30003
	v_and_b32_e32 v9, 0x7c, v3
	v_sub_u32_e32 v3, v0, v11
	s_add_u32 s0, s72, s76
	v_lshlrev_b32_e32 v3, 2, v3
	v_or_b32_e32 v166, 2, v159
	v_writelane_b32 v252, s0, 4
	s_addc_u32 s0, s73, s77
	v_and_b32_e32 v12, 0x7c, v3
	v_sub_u32_e32 v3, v0, v166
	v_writelane_b32 v252, s0, 5
	s_lshl_b32 s0, s41, 12
	v_lshlrev_b32_e32 v3, 2, v3
	v_or_b32_e32 v167, 3, v159
	s_lshl_b64 s[2:3], s[38:39], 11
	v_bfe_u32 v5, v0, 4, 2
	s_bfe_u32 s39, s1, 0x20006
	s_add_i32 s0, s0, 0x20000
	v_and_b32_e32 v14, 0x7c, v3
	v_sub_u32_e32 v3, v0, v167
	v_xor_b32_e32 v28, v5, v0
	v_bitop3_b32 v5, v5, v0, 4 bitop3:0x36
	v_writelane_b32 v252, s5, 6
	s_xor_b32 s5, s5, 15
	s_lshl_b32 s48, s39, 5
	v_lshlrev_b32_e32 v3, 2, v3
	v_or_b32_e32 v168, 8, v159
	v_pack_b32_f16 v118, v2, 0
	v_bfe_u32 v2, v0, 3, 3
	v_lshlrev_b32_e32 v28, 4, v28
	v_lshlrev_b32_e32 v5, 4, v5
	s_cmpk_lt_u32 s1, 0x100
	v_and_b32_e32 v16, 0x7c, v3
	v_sub_u32_e32 v3, v0, v168
	v_lshlrev_b32_e32 v27, 7, v2
	v_and_b32_e32 v28, 0x70, v28
	v_and_b32_e32 v5, 0x70, v5
	v_writelane_b32 v252, s5, 7
	s_cselect_b64 s[44:45], -1, 0
	s_lshl_b32 s5, s39, 1
	v_and_b32_e32 v6, 31, v0
	v_lshlrev_b32_e32 v3, 2, v3
	v_or_b32_e32 v169, 9, v159
	v_lshlrev_b32_e32 v2, 12, v2
	v_or_b32_e32 v172, v28, v27
	v_or_b32_e32 v174, v5, v27
	v_lshlrev_b32_e32 v27, 3, v0
	v_writelane_b32 v252, s5, 8
	s_or_b32 s5, s5, 1
	v_and_b32_e32 v18, 0x7c, v3
	v_sub_u32_e32 v3, v0, v169
	v_lshlrev_b32_e32 v26, 9, v4
	v_or_b32_e32 v173, v28, v2
	v_or_b32_e32 v175, v5, v2
	v_and_b32_e32 v28, 0x70, v27
	s_lshl_b32 s6, s5, 10
	v_writelane_b32 v252, s5, 9
	s_lshl_b32 s5, s5, 15
	v_or_b32_e32 v158, s2, v6
	v_lshlrev_b32_e32 v2, 3, v4
	v_lshlrev_b32_e32 v4, 4, v4
	s_movk_i32 s2, 0x60
	v_lshlrev_b32_e32 v3, 2, v3
	v_or_b32_e32 v170, 10, v159
	v_writelane_b32 v252, s5, 10
	v_bitop3_b32 v180, v4, v28, s2 bitop3:0x36
	s_bfe_u32 s2, s41, 0x10001
	v_and_b32_e32 v20, 0x7c, v3
	v_sub_u32_e32 v3, v0, v170
	s_lshl_b32 s50, s39, 11
	v_writelane_b32 v252, s6, 11
	s_or_b32 s2, s2, -6
	v_lshlrev_b32_e32 v3, 2, v3
	v_or_b32_e32 v171, 11, v159
	v_writelane_b32 v252, s2, 12
	s_and_b32 s2, s50, 0x800
	v_and_b32_e32 v22, 0x7c, v3
	v_sub_u32_e32 v3, v0, v171
	v_lshlrev_b32_e32 v29, 4, v1
	s_or_b32 s2, s40, s2
	v_lshlrev_b32_e32 v3, 2, v3
	s_lshl_b32 s49, s39, 16
	s_or_b32 s1, s40, s50
	s_or_b32 s42, s40, s6
	v_mov_b32_e32 v1, s3
	s_or_b32 s3, s50, 0x1000
	v_or_b32_e32 v190, s2, v29
	s_or_b32 s2, s50, 0x1400
	v_and_b32_e32 v24, 0x7c, v3
	v_mov_b32_e32 v3, 0
	v_writelane_b32 v252, s3, 13
	s_cmp_eq_u32 s33, 1
	s_movk_i32 s4, 0x70
	v_mov_b32_e32 v5, v3
	v_writelane_b32 v252, s2, 14
	s_cselect_b64 s[2:3], -1, 0
	v_lshl_add_u64 v[160:161], s[68:69], 0, v[4:5]
	v_bitop3_b32 v177, v4, v27, s4 bitop3:0x78
	v_bitop3_b32 v178, v4, v28, 32 bitop3:0x36
	v_bitop3_b32 v179, v4, v28, 64 bitop3:0x36
	v_writelane_b32 v252, s2, 15
	v_mov_b32_e32 v4, 2
	v_lshlrev_b32_sdwa v207, v4, v0 dst_sel:DWORD dst_unused:UNUSED_PAD src0_sel:DWORD src1_sel:BYTE_0
	v_writelane_b32 v252, s3, 16
	s_lshl_b32 s2, s38, 7
	v_mov_b32_e32 v4, 0x7ffff81f
	v_bitop3_b32 v0, s2, v4, v0 bitop3:0xc8
	s_and_b32 s2, s2, 0x780
	s_add_u32 s2, s36, s2
	s_addc_u32 s3, s37, 0
	v_lshl_add_u64 v[162:163], s[2:3], 0, v[2:3]
	s_or_b32 s2, s49, 0x8080
	v_writelane_b32 v252, s2, 17
	s_or_b32 s2, s49, 0x80
	s_lshl_b32 s51, s39, 12
	v_writelane_b32 v252, s2, 18
	s_or_b32 s2, s50, 0x2000
	v_writelane_b32 v252, s2, 19
	s_add_u32 s2, s70, 0x400
	v_writelane_b32 v252, s2, 20
	s_addc_u32 s2, s71, 0
	v_writelane_b32 v252, s2, 21
	s_or_b32 s2, s50, 0x4000
	v_writelane_b32 v252, s2, 22
	s_add_u32 s2, s70, 0x4000
	v_writelane_b32 v252, s2, 23
	s_addc_u32 s2, s71, 0
	v_writelane_b32 v252, s2, 24
	s_or_b32 s2, s49, 0x8100
	v_writelane_b32 v252, s2, 25
	s_add_u32 s2, s72, 0x100
	v_writelane_b32 v252, s2, 26
	s_addc_u32 s2, s73, 0
	v_writelane_b32 v252, s2, 27
	v_writelane_b32 v252, s44, 28
	v_cmp_gt_u32_e64 s[52:53], v6, v159
	v_lshlrev_b32_e32 v7, 2, v6
	v_writelane_b32 v252, s45, 29
	v_writelane_b32 v252, s52, 30
	v_lshlrev_b32_e32 v8, 7, v6
	v_or_b32_e32 v10, v9, v8
	v_writelane_b32 v252, s53, 31
	v_writelane_b32 v252, s51, 32
	v_or_b32_e32 v13, v12, v8
	v_or_b32_e32 v15, v14, v8
	v_or_b32_e32 v17, v16, v8
	v_or_b32_e32 v19, v18, v8
	v_or_b32_e32 v21, v20, v8
	v_or_b32_e32 v23, v22, v8
	v_or_b32_e32 v25, v24, v8
	v_or_b32_e32 v176, s40, v8
	v_or3_b32 v181, s0, v26, v7
	v_cmp_gt_u32_e64 s[4:5], v6, v11
	v_or_b32_e32 v182, 16, v159
	v_or_b32_e32 v183, 17, v159
	v_or_b32_e32 v184, 18, v159
	v_or_b32_e32 v185, 19, v159
	v_or_b32_e32 v186, 24, v159
	v_or_b32_e32 v187, 25, v159
	v_or_b32_e32 v188, 26, v159
	v_or_b32_e32 v189, 27, v159
	v_bitop3_b32 v4, v9, 64, v8 bitop3:0x36
	v_bitop3_b32 v5, v12, 64, v8 bitop3:0x36
	v_bitop3_b32 v7, v14, 64, v8 bitop3:0x36
	v_bitop3_b32 v9, v16, 64, v8 bitop3:0x36
	v_bitop3_b32 v11, v18, 64, v8 bitop3:0x36
	v_bitop3_b32 v12, v20, 64, v8 bitop3:0x36
	v_bitop3_b32 v14, v22, 64, v8 bitop3:0x36
	v_bitop3_b32 v8, v24, 64, v8 bitop3:0x36
	v_add_u32_e32 v210, s1, v29
	v_add_u32_e32 v212, s42, v29
	v_writelane_b32 v252, s48, 33
	v_mov_b32_e32 v119, v3
	v_mov_b32_e32 v120, v3
	v_mov_b32_e32 v121, v3
	v_cmp_gt_u32_e64 s[6:7], v6, v166
	v_cmp_gt_u32_e64 s[8:9], v6, v167
	v_cmp_gt_u32_e64 s[10:11], v6, v168
	v_cmp_gt_u32_e64 s[12:13], v6, v169
	v_cmp_gt_u32_e64 s[14:15], v6, v170
	v_cmp_gt_u32_e64 s[16:17], v6, v171
	v_cmp_gt_u32_e64 s[18:19], v6, v182
	v_cmp_gt_u32_e64 s[20:21], v6, v183
	v_cmp_gt_u32_e64 s[22:23], v6, v184
	v_cmp_gt_u32_e64 s[24:25], v6, v185
	v_cmp_gt_u32_e64 s[26:27], v6, v186
	v_cmp_gt_u32_e64 s[28:29], v6, v187
	v_cmp_gt_u32_e64 s[30:31], v6, v188
	v_cmp_gt_u32_e64 s[34:35], v6, v189
	v_or_b32_e32 v191, 32, v159
	v_or_b32_e32 v192, 33, v159
	v_or_b32_e32 v193, 34, v159
	v_or_b32_e32 v194, 35, v159
	v_or_b32_e32 v195, 40, v159
	v_or_b32_e32 v196, 41, v159
	v_or_b32_e32 v197, 42, v159
	v_or_b32_e32 v198, 43, v159
	v_or_b32_e32 v199, 48, v159
	v_or_b32_e32 v200, 49, v159
	v_or_b32_e32 v201, 50, v159
	v_or_b32_e32 v202, 51, v159
	v_or_b32_e32 v203, 56, v159
	v_or_b32_e32 v204, 57, v159
	v_or_b32_e32 v205, 58, v159
	v_or_b32_e32 v206, 59, v159
	v_or_b32_e32 v208, s40, v29
	v_or_b32_e32 v209, s48, v6
	s_mov_b64 s[38:39], -1
	v_add_u32_e32 v211, 0x4000, v210
	v_add_u32_e32 v213, 0x4000, v212
	v_add_u32_e32 v214, s0, v10
	v_add_u32_e32 v215, s0, v13
	v_add_u32_e32 v216, s0, v15
	v_add_u32_e32 v217, s0, v17
	v_add_u32_e32 v218, s0, v19
	v_add_u32_e32 v219, s0, v21
	v_add_u32_e32 v220, s0, v23
	v_add_u32_e32 v221, s0, v25
	v_add_u32_e32 v222, s0, v4
	v_add_u32_e32 v223, s0, v5
	v_add_u32_e32 v224, s0, v7
	v_add_u32_e32 v225, s0, v9
	v_add_u32_e32 v226, s0, v11
	v_add_u32_e32 v227, s0, v12
	v_add_u32_e32 v228, s0, v14
	v_add_u32_e32 v229, s0, v8
	v_mov_b32_e32 v230, 0xf149f2ca
	v_mov_b32_e32 v231, 0x8000
	v_writelane_b32 v252, s49, 34
	v_writelane_b32 v252, s50, 35
	s_branch .LBB2_2

	.amdhsa_kernel _Z11attn_kernelPKDF16_S0_S0_S0_PDF16_
		.amdhsa_group_segment_fixed_size 163840
		.amdhsa_private_segment_fixed_size 0
		.amdhsa_kernarg_size 40
		.amdhsa_user_sgpr_count 2
		.amdhsa_user_sgpr_dispatch_ptr 0
		.amdhsa_user_sgpr_queue_ptr 0
		.amdhsa_user_sgpr_kernarg_segment_ptr 1
		.amdhsa_user_sgpr_dispatch_id 0
		.amdhsa_user_sgpr_kernarg_preload_length 0
		.amdhsa_user_sgpr_kernarg_preload_offset 0
		.amdhsa_user_sgpr_private_segment_size 0
		.amdhsa_uses_dynamic_stack 0
		.amdhsa_enable_private_segment 0
		.amdhsa_system_sgpr_workgroup_id_x 1
		.amdhsa_system_sgpr_workgroup_id_y 0
		.amdhsa_system_sgpr_workgroup_id_z 0
		.amdhsa_system_sgpr_workgroup_info 0
		.amdhsa_system_vgpr_workitem_id 0
		.amdhsa_next_free_vgpr 256
		.amdhsa_next_free_sgpr 102
		.amdhsa_accum_offset 256
		.amdhsa_reserve_vcc 1
		.amdhsa_float_round_mode_32 0
		.amdhsa_float_round_mode_16_64 0
		.amdhsa_float_denorm_mode_32 3
		.amdhsa_float_denorm_mode_16_64 3
		.amdhsa_dx10_clamp 1
		.amdhsa_ieee_mode 1
		.amdhsa_fp16_overflow 0
		.amdhsa_tg_split 0
		.amdhsa_exception_fp_ieee_invalid_op 0
		.amdhsa_exception_fp_denorm_src 0
		.amdhsa_exception_fp_ieee_div_zero 0
		.amdhsa_exception_fp_ieee_overflow 0
		.amdhsa_exception_fp_ieee_underflow 0
		.amdhsa_exception_fp_ieee_inexact 0
		.amdhsa_exception_int_div_zero 0
	.end_amdhsa_kernel
